# speedup vs baseline: 1.0061x; 1.0042x over previous
.Lpre_roleE:
	s_sub_u32 s3, s2, 0xad
	s_cmp_gt_u32 s3, 191
	s_cbranch_scc1 .Lpre_E_exit
	s_load_dwordx16 s[4:19], s[0:1], 0x68
	s_load_dwordx2 s[20:21], s[0:1], 0xa8
	s_mul_hi_u32 s22, s3, 0xaaaaaaab
	s_lshr_b32 s22, s22, 3
	s_mul_i32 s23, s22, 12
	s_sub_u32 s23, s3, s23
	s_lshr_b32 s24, s23, 2
	s_and_b32 s25, s23, 3
	s_lshl_b32 s25, s25, 6
	v_and_b32_e32 v1, 63, v0
	v_lshrrev_b32_e32 v62, 6, v0
	v_and_b32_e32 v2, 15, v0
	v_bfe_u32 v3, v0, 4, 2
	v_readfirstlane_b32 s26, v62
	s_cmp_lt_u32 s24, 2
	s_cselect_b32 s28, 14, 13
	s_lshl_b32 s27, 1, s28
	s_lshr_b32 s27, s27, 3
	v_lshlrev_b32_e32 v4, s28, v3
	v_lshl_or_b32 v4, v62, 6, v4
	v_lshl_or_b32 v4, v2, 2, v4
	v_add_u32_e32 v5, s27, v4
	v_add_u32_e32 v6, s27, v5
	v_add_u32_e32 v7, s27, v6
	v_add_u32_e32 v8, s27, v7
	v_add_u32_e32 v9, s27, v8
	v_add_u32_e32 v10, s27, v9
	v_add_u32_e32 v11, s27, v10
	v_lshlrev_b32_e32 v12, 4, v1
	v_add_u32_e32 v13, 0x1000, v12
	s_lshl_b32 s29, s22, 15
	s_lshl_b32 s30, s26, 13
	s_add_u32 s29, s29, s30
	s_waitcnt lgkmcnt(0)
	s_add_u32 s32, s4, s29
	s_addc_u32 s33, s5, 0
	global_load_dwordx4 v[16:19], v12, s[32:33]
	global_load_dwordx4 v[20:23], v12, s[32:33] offset:1024
	global_load_dwordx4 v[24:27], v12, s[32:33] offset:2048
	global_load_dwordx4 v[28:31], v12, s[32:33] offset:3072
	global_load_dwordx4 v[32:35], v13, s[32:33]
	global_load_dwordx4 v[36:39], v13, s[32:33] offset:1024
	global_load_dwordx4 v[40:43], v13, s[32:33] offset:2048
	global_load_dwordx4 v[44:47], v13, s[32:33] offset:3072
	global_load_dwordx4 v[48:51], v12, s[6:7]
	global_load_dwordx4 v[52:55], v12, s[8:9]
	s_cmp_lt_u32 s24, 2
	s_cselect_b32 s34, s10, s12
	s_cselect_b32 s35, s11, s13
	s_and_b32 s36, s24, 1
	s_lshl_b32 s36, s36, 10
	s_lshl_b32 s37, s25, 2
	s_add_u32 s36, s36, s37
	s_add_u32 s34, s34, s36
	s_addc_u32 s35, s35, 0
	s_lshl_b32 s38, s27, 5
	s_mov_b64 s[40:41], s[34:35]
	s_add_u32 s42, s40, s38
	s_addc_u32 s43, s41, 0
	s_add_u32 s44, s42, s38
	s_addc_u32 s45, s43, 0
	s_add_u32 s46, s44, s38
	s_addc_u32 s47, s45, 0
	s_add_u32 s48, s46, s38
	s_addc_u32 s49, s47, 0
	s_add_u32 s50, s48, s38
	s_addc_u32 s51, s49, 0
	s_add_u32 s52, s50, s38
	s_addc_u32 s53, s51, 0
	s_add_u32 s54, s52, s38
	s_addc_u32 s55, s53, 0
	global_load_dword v64, v4, s[40:41]
	global_load_dword v65, v5, s[40:41]
	global_load_dword v66, v6, s[40:41]
	global_load_dword v67, v7, s[40:41]
	global_load_dword v68, v8, s[40:41]
	global_load_dword v69, v9, s[40:41]
	global_load_dword v70, v10, s[40:41]
	global_load_dword v71, v11, s[40:41]
	global_load_dword v72, v4, s[42:43]
	global_load_dword v73, v5, s[42:43]
	global_load_dword v74, v6, s[42:43]
	global_load_dword v75, v7, s[42:43]
	global_load_dword v76, v8, s[42:43]
	global_load_dword v77, v9, s[42:43]
	global_load_dword v78, v10, s[42:43]
	global_load_dword v79, v11, s[42:43]
	global_load_dword v80, v4, s[44:45]
	global_load_dword v81, v5, s[44:45]
	global_load_dword v82, v6, s[44:45]
	global_load_dword v83, v7, s[44:45]
	global_load_dword v84, v8, s[44:45]
	global_load_dword v85, v9, s[44:45]
	global_load_dword v86, v10, s[44:45]
	global_load_dword v87, v11, s[44:45]
	global_load_dword v88, v4, s[46:47]
	global_load_dword v89, v5, s[46:47]
	global_load_dword v90, v6, s[46:47]
	global_load_dword v91, v7, s[46:47]
	global_load_dword v92, v8, s[46:47]
	global_load_dword v93, v9, s[46:47]
	global_load_dword v94, v10, s[46:47]
	global_load_dword v95, v11, s[46:47]
	global_load_dword v96, v4, s[48:49]
	global_load_dword v97, v5, s[48:49]
	global_load_dword v98, v6, s[48:49]
	global_load_dword v99, v7, s[48:49]
	global_load_dword v100, v8, s[48:49]
	global_load_dword v101, v9, s[48:49]
	global_load_dword v102, v10, s[48:49]
	global_load_dword v103, v11, s[48:49]
	global_load_dword v104, v4, s[50:51]
	global_load_dword v105, v5, s[50:51]
	global_load_dword v106, v6, s[50:51]
	global_load_dword v107, v7, s[50:51]
	global_load_dword v108, v8, s[50:51]
	global_load_dword v109, v9, s[50:51]
	global_load_dword v110, v10, s[50:51]
	global_load_dword v111, v11, s[50:51]
	global_load_dword v112, v4, s[52:53]
	global_load_dword v113, v5, s[52:53]
	global_load_dword v114, v6, s[52:53]
	global_load_dword v115, v7, s[52:53]
	global_load_dword v116, v8, s[52:53]
	global_load_dword v117, v9, s[52:53]
	global_load_dword v118, v10, s[52:53]
	global_load_dword v119, v11, s[52:53]
	global_load_dword v120, v4, s[54:55]
	global_load_dword v121, v5, s[54:55]
	global_load_dword v122, v6, s[54:55]
	global_load_dword v123, v7, s[54:55]
	global_load_dword v124, v8, s[54:55]
	global_load_dword v125, v9, s[54:55]
	global_load_dword v126, v10, s[54:55]
	global_load_dword v127, v11, s[54:55]
	v_lshlrev_b32_e32 v14, 6, v62
	v_lshl_or_b32 v14, v3, 4, v14
	s_lshl_b32 s37, s25, 2
	s_add_u32 s56, s14, s37
	s_addc_u32 s57, s15, 0
	s_waitcnt vmcnt(63)
	v_add_f32_e32 v4, v16, v17
	v_add_f32_e32 v5, v20, v21
	v_add_f32_e32 v6, v24, v25
	v_add_f32_e32 v7, v28, v29
	v_add_f32_e32 v8, v32, v33
	v_add_f32_e32 v9, v36, v37
	v_add_f32_e32 v10, v40, v41
	v_add_f32_e32 v11, v44, v45
	v_mul_f32_e32 v56, v16, v16
	v_mul_f32_e32 v57, v20, v20
	v_mul_f32_e32 v58, v24, v24
	v_mul_f32_e32 v59, v28, v28
	v_mul_f32_e32 v60, v32, v32
	v_mul_f32_e32 v61, v36, v36
	v_mul_f32_e32 v63, v40, v40
	v_mul_f32_e32 v15, v44, v44
	v_add_f32_e32 v4, v4, v18
	v_add_f32_e32 v5, v5, v22
	v_add_f32_e32 v6, v6, v26
	v_add_f32_e32 v7, v7, v30
	v_add_f32_e32 v8, v8, v34
	v_add_f32_e32 v9, v9, v38
	v_add_f32_e32 v10, v10, v42
	v_add_f32_e32 v11, v11, v46
	v_fmac_f32_e32 v56, v17, v17
	v_fmac_f32_e32 v57, v21, v21
	v_fmac_f32_e32 v58, v25, v25
	v_fmac_f32_e32 v59, v29, v29
	v_fmac_f32_e32 v60, v33, v33
	v_fmac_f32_e32 v61, v37, v37
	v_fmac_f32_e32 v63, v41, v41
	v_fmac_f32_e32 v15, v45, v45
	v_add_f32_e32 v4, v4, v19
	v_add_f32_e32 v5, v5, v23
	v_add_f32_e32 v6, v6, v27
	v_add_f32_e32 v7, v7, v31
	v_add_f32_e32 v8, v8, v35
	v_add_f32_e32 v9, v9, v39
	v_add_f32_e32 v10, v10, v43
	v_add_f32_e32 v11, v11, v47
	v_fmac_f32_e32 v56, v18, v18
	v_fmac_f32_e32 v57, v22, v22
	v_fmac_f32_e32 v58, v26, v26
	v_fmac_f32_e32 v59, v30, v30
	v_fmac_f32_e32 v60, v34, v34
	v_fmac_f32_e32 v61, v38, v38
	v_fmac_f32_e32 v63, v42, v42
	v_fmac_f32_e32 v15, v46, v46
	v_fmac_f32_e32 v56, v19, v19
	v_fmac_f32_e32 v57, v23, v23
	v_fmac_f32_e32 v58, v27, v27
	v_fmac_f32_e32 v59, v31, v31
	v_fmac_f32_e32 v60, v35, v35
	v_fmac_f32_e32 v61, v39, v39
	v_fmac_f32_e32 v63, v43, v43
	v_fmac_f32_e32 v15, v47, v47
	s_nop 1
	v_permlane32_swap_b32_e32 v4, v56
	v_permlane32_swap_b32_e32 v5, v57
	v_permlane32_swap_b32_e32 v6, v58
	v_permlane32_swap_b32_e32 v7, v59
	v_permlane32_swap_b32_e32 v8, v60
	v_permlane32_swap_b32_e32 v9, v61
	v_permlane32_swap_b32_e32 v10, v63
	v_permlane32_swap_b32_e32 v11, v15
	v_add_f32_e32 v4, v4, v56
	v_add_f32_e32 v5, v5, v57
	v_add_f32_e32 v6, v6, v58
	v_add_f32_e32 v7, v7, v59
	v_add_f32_e32 v8, v8, v60
	v_add_f32_e32 v9, v9, v61
	v_add_f32_e32 v10, v10, v63
	v_add_f32_e32 v11, v11, v15
	s_nop 1
	v_permlane16_swap_b32_e32 v4, v5
	v_permlane16_swap_b32_e32 v6, v7
	v_permlane16_swap_b32_e32 v8, v9
	v_permlane16_swap_b32_e32 v10, v11
	v_add_f32_e32 v4, v4, v5
	v_add_f32_e32 v6, v6, v7
	v_add_f32_e32 v8, v8, v9
	v_add_f32_e32 v10, v10, v11
	s_nop 1
	v_add_f32_dpp v4, v4, v4 quad_perm:[1,0,3,2] row_mask:0xf bank_mask:0xf
	v_add_f32_dpp v6, v6, v6 quad_perm:[1,0,3,2] row_mask:0xf bank_mask:0xf
	v_add_f32_dpp v8, v8, v8 quad_perm:[1,0,3,2] row_mask:0xf bank_mask:0xf
	v_add_f32_dpp v10, v10, v10 quad_perm:[1,0,3,2] row_mask:0xf bank_mask:0xf
	s_nop 0
	v_add_f32_dpp v4, v4, v4 quad_perm:[2,3,0,1] row_mask:0xf bank_mask:0xf
	v_add_f32_dpp v6, v6, v6 quad_perm:[2,3,0,1] row_mask:0xf bank_mask:0xf
	v_add_f32_dpp v8, v8, v8 quad_perm:[2,3,0,1] row_mask:0xf bank_mask:0xf
	v_add_f32_dpp v10, v10, v10 quad_perm:[2,3,0,1] row_mask:0xf bank_mask:0xf
	s_nop 0
	v_add_f32_dpp v4, v4, v4 row_half_mirror row_mask:0xf bank_mask:0xf
	v_add_f32_dpp v6, v6, v6 row_half_mirror row_mask:0xf bank_mask:0xf
	v_add_f32_dpp v8, v8, v8 row_half_mirror row_mask:0xf bank_mask:0xf
	v_add_f32_dpp v10, v10, v10 row_half_mirror row_mask:0xf bank_mask:0xf
	s_nop 0
	v_add_f32_dpp v4, v4, v4 row_mirror row_mask:0xf bank_mask:0xf
	v_add_f32_dpp v6, v6, v6 row_mirror row_mask:0xf bank_mask:0xf
	v_add_f32_dpp v8, v8, v8 row_mirror row_mask:0xf bank_mask:0xf
	v_add_f32_dpp v10, v10, v10 row_mirror row_mask:0xf bank_mask:0xf
	s_nop 0
	v_mov_b32_e32 v5, v4
	v_mov_b32_e32 v7, v6
	v_mov_b32_e32 v9, v8
	v_mov_b32_e32 v11, v10
	s_nop 1
	v_permlane32_swap_b32_e32 v4, v5
	v_permlane32_swap_b32_e32 v6, v7
	v_permlane32_swap_b32_e32 v8, v9
	v_permlane32_swap_b32_e32 v10, v11
	v_mov_b32_e32 v60, 0x3727c5ac
	v_mul_f32_e32 v4, 0x3b800000, v4
	v_mul_f32_e32 v6, 0x3b800000, v6
	v_mul_f32_e32 v8, 0x3b800000, v8
	v_mul_f32_e32 v10, 0x3b800000, v10
	v_mul_f32_e32 v5, 0x3b800000, v5
	v_mul_f32_e32 v7, 0x3b800000, v7
	v_mul_f32_e32 v9, 0x3b800000, v9
	v_mul_f32_e32 v11, 0x3b800000, v11
	v_add_f32_e32 v5, v5, v60
	v_add_f32_e32 v7, v7, v60
	v_add_f32_e32 v9, v9, v60
	v_add_f32_e32 v11, v11, v60
	v_fma_f32 v5, -v4, v4, v5
	v_fma_f32 v7, -v6, v6, v7
	v_fma_f32 v9, -v8, v8, v9
	v_fma_f32 v11, -v10, v10, v11
	v_rsq_f32_e32 v5, v5
	v_rsq_f32_e32 v7, v7
	v_rsq_f32_e32 v9, v9
	v_rsq_f32_e32 v11, v11
	s_nop 1
	v_readlane_b32 s64, v4, 0
	v_readlane_b32 s65, v5, 0
	v_readlane_b32 s66, v4, 16
	v_readlane_b32 s67, v5, 16
	v_readlane_b32 s68, v6, 0
	v_readlane_b32 s69, v7, 0
	v_readlane_b32 s70, v6, 16
	v_readlane_b32 s71, v7, 16
	v_readlane_b32 s72, v8, 0
	v_readlane_b32 s73, v9, 0
	v_readlane_b32 s74, v8, 16
	v_readlane_b32 s75, v9, 16
	v_readlane_b32 s76, v10, 0
	v_readlane_b32 s77, v11, 0
	v_readlane_b32 s78, v10, 16
	v_readlane_b32 s79, v11, 16
	s_nop 1
	v_subrev_f32_e32 v16, s64, v16
	v_subrev_f32_e32 v17, s64, v17
	v_subrev_f32_e32 v18, s64, v18
	v_subrev_f32_e32 v19, s64, v19
	v_mul_f32_e32 v16, s65, v16
	v_mul_f32_e32 v17, s65, v17
	v_mul_f32_e32 v18, s65, v18
	v_mul_f32_e32 v19, s65, v19
	v_subrev_f32_e32 v20, s66, v20
	v_subrev_f32_e32 v21, s66, v21
	v_subrev_f32_e32 v22, s66, v22
	v_subrev_f32_e32 v23, s66, v23
	v_mul_f32_e32 v20, s67, v20
	v_mul_f32_e32 v21, s67, v21
	v_mul_f32_e32 v22, s67, v22
	v_mul_f32_e32 v23, s67, v23
	v_subrev_f32_e32 v24, s68, v24
	v_subrev_f32_e32 v25, s68, v25
	v_subrev_f32_e32 v26, s68, v26
	v_subrev_f32_e32 v27, s68, v27
	v_mul_f32_e32 v24, s69, v24
	v_mul_f32_e32 v25, s69, v25
	v_mul_f32_e32 v26, s69, v26
	v_mul_f32_e32 v27, s69, v27
	v_subrev_f32_e32 v28, s70, v28
	v_subrev_f32_e32 v29, s70, v29
	v_subrev_f32_e32 v30, s70, v30
	v_subrev_f32_e32 v31, s70, v31
	v_mul_f32_e32 v28, s71, v28
	v_mul_f32_e32 v29, s71, v29
	v_mul_f32_e32 v30, s71, v30
	v_mul_f32_e32 v31, s71, v31
	v_subrev_f32_e32 v32, s72, v32
	v_subrev_f32_e32 v33, s72, v33
	v_subrev_f32_e32 v34, s72, v34
	v_subrev_f32_e32 v35, s72, v35
	v_mul_f32_e32 v32, s73, v32
	v_mul_f32_e32 v33, s73, v33
	v_mul_f32_e32 v34, s73, v34
	v_mul_f32_e32 v35, s73, v35
	v_subrev_f32_e32 v36, s74, v36
	v_subrev_f32_e32 v37, s74, v37
	v_subrev_f32_e32 v38, s74, v38
	v_subrev_f32_e32 v39, s74, v39
	v_mul_f32_e32 v36, s75, v36
	v_mul_f32_e32 v37, s75, v37
	v_mul_f32_e32 v38, s75, v38
	v_mul_f32_e32 v39, s75, v39
	v_subrev_f32_e32 v40, s76, v40
	v_subrev_f32_e32 v41, s76, v41
	v_subrev_f32_e32 v42, s76, v42
	v_subrev_f32_e32 v43, s76, v43
	v_mul_f32_e32 v40, s77, v40
	v_mul_f32_e32 v41, s77, v41
	v_mul_f32_e32 v42, s77, v42
	v_mul_f32_e32 v43, s77, v43
	v_subrev_f32_e32 v44, s78, v44
	v_subrev_f32_e32 v45, s78, v45
	v_subrev_f32_e32 v46, s78, v46
	v_subrev_f32_e32 v47, s78, v47
	v_mul_f32_e32 v44, s79, v44
	v_mul_f32_e32 v45, s79, v45
	v_mul_f32_e32 v46, s79, v46
	v_mul_f32_e32 v47, s79, v47
	v_fma_f32 v16, v16, v48, v52
	v_fma_f32 v17, v17, v49, v53
	v_fma_f32 v18, v18, v50, v54
	v_fma_f32 v19, v19, v51, v55
	v_fma_f32 v20, v20, v48, v52
	v_fma_f32 v21, v21, v49, v53
	v_fma_f32 v22, v22, v50, v54
	v_fma_f32 v23, v23, v51, v55
	v_fma_f32 v24, v24, v48, v52
	v_fma_f32 v25, v25, v49, v53
	v_fma_f32 v26, v26, v50, v54
	v_fma_f32 v27, v27, v51, v55
	v_fma_f32 v28, v28, v48, v52
	v_fma_f32 v29, v29, v49, v53
	v_fma_f32 v30, v30, v50, v54
	v_fma_f32 v31, v31, v51, v55
	v_fma_f32 v32, v32, v48, v52
	v_fma_f32 v33, v33, v49, v53
	v_fma_f32 v34, v34, v50, v54
	v_fma_f32 v35, v35, v51, v55
	v_fma_f32 v36, v36, v48, v52
	v_fma_f32 v37, v37, v49, v53
	v_fma_f32 v38, v38, v50, v54
	v_fma_f32 v39, v39, v51, v55
	v_fma_f32 v40, v40, v48, v52
	v_fma_f32 v41, v41, v49, v53
	v_fma_f32 v42, v42, v50, v54
	v_fma_f32 v43, v43, v51, v55
	v_fma_f32 v44, v44, v48, v52
	v_fma_f32 v45, v45, v49, v53
	v_fma_f32 v46, v46, v50, v54
	v_fma_f32 v47, v47, v51, v55
	global_load_dwordx4 v[56:59], v14, s[56:57]
	v_lshlrev_b32_e32 v61, 3, v1
	s_mul_i32 s31, s26, 4224
	v_add_u32_e32 v61, s31, v61
	v_cvt_pk_bf16_f32 v16, v16, v17
	v_cvt_pk_bf16_f32 v17, v18, v19
	ds_write_b64 v61, v[16:17]
	v_cvt_pk_bf16_f32 v20, v20, v21
	v_cvt_pk_bf16_f32 v21, v22, v23
	ds_write_b64 v61, v[20:21] offset:528
	v_cvt_pk_bf16_f32 v24, v24, v25
	v_cvt_pk_bf16_f32 v25, v26, v27
	ds_write_b64 v61, v[24:25] offset:1056
	v_cvt_pk_bf16_f32 v28, v28, v29
	v_cvt_pk_bf16_f32 v29, v30, v31
	ds_write_b64 v61, v[28:29] offset:1584
	v_cvt_pk_bf16_f32 v32, v32, v33
	v_cvt_pk_bf16_f32 v33, v34, v35
	ds_write_b64 v61, v[32:33] offset:2112
	v_cvt_pk_bf16_f32 v36, v36, v37
	v_cvt_pk_bf16_f32 v37, v38, v39
	ds_write_b64 v61, v[36:37] offset:2640
	v_cvt_pk_bf16_f32 v40, v40, v41
	v_cvt_pk_bf16_f32 v41, v42, v43
	ds_write_b64 v61, v[40:41] offset:3168
	v_cvt_pk_bf16_f32 v44, v44, v45
	v_cvt_pk_bf16_f32 v45, v46, v47
	ds_write_b64 v61, v[44:45] offset:3696
	v_mul_u32_u24_e32 v63, 528, v2
	v_lshlrev_b32_e32 v60, 4, v3
	v_add_u32_e32 v63, v63, v60
	s_waitcnt lgkmcnt(0)
	s_barrier
	s_waitcnt vmcnt(1)
	v_cvt_pk_bf16_f32 v64, v64, v65
	v_cvt_pk_bf16_f32 v65, v66, v67
	v_cvt_pk_bf16_f32 v66, v68, v69
	v_cvt_pk_bf16_f32 v67, v70, v71
	v_cvt_pk_bf16_f32 v72, v72, v73
	v_cvt_pk_bf16_f32 v73, v74, v75
	v_cvt_pk_bf16_f32 v74, v76, v77
	v_cvt_pk_bf16_f32 v75, v78, v79
	v_cvt_pk_bf16_f32 v80, v80, v81
	v_cvt_pk_bf16_f32 v81, v82, v83
	v_cvt_pk_bf16_f32 v82, v84, v85
	v_cvt_pk_bf16_f32 v83, v86, v87
	v_cvt_pk_bf16_f32 v88, v88, v89
	v_cvt_pk_bf16_f32 v89, v90, v91
	v_cvt_pk_bf16_f32 v90, v92, v93
	v_cvt_pk_bf16_f32 v91, v94, v95
	v_cvt_pk_bf16_f32 v96, v96, v97
	v_cvt_pk_bf16_f32 v97, v98, v99
	v_cvt_pk_bf16_f32 v98, v100, v101
	v_cvt_pk_bf16_f32 v99, v102, v103
	v_cvt_pk_bf16_f32 v104, v104, v105
	v_cvt_pk_bf16_f32 v105, v106, v107
	v_cvt_pk_bf16_f32 v106, v108, v109
	v_cvt_pk_bf16_f32 v107, v110, v111
	v_cvt_pk_bf16_f32 v112, v112, v113
	v_cvt_pk_bf16_f32 v113, v114, v115
	v_cvt_pk_bf16_f32 v114, v116, v117
	v_cvt_pk_bf16_f32 v115, v118, v119
	v_cvt_pk_bf16_f32 v120, v120, v121
	v_cvt_pk_bf16_f32 v121, v122, v123
	v_cvt_pk_bf16_f32 v122, v124, v125
	v_cvt_pk_bf16_f32 v123, v126, v127
	ds_read_b128 v[16:19], v63 offset:0
	ds_read_b128 v[20:23], v63 offset:8448
	ds_read_b128 v[24:27], v63 offset:64
	ds_read_b128 v[28:31], v63 offset:8512
	ds_read_b128 v[32:35], v63 offset:128
	ds_read_b128 v[36:39], v63 offset:8576
	ds_read_b128 v[40:43], v63 offset:192
	ds_read_b128 v[44:47], v63 offset:8640
	s_waitcnt lgkmcnt(0)
	v_mfma_f32_16x16x32_bf16 v[48:51], v[64:67], v[16:19], 0
	v_mfma_f32_16x16x32_bf16 v[52:55], v[64:67], v[20:23], 0
	v_mfma_f32_16x16x32_bf16 v[48:51], v[72:75], v[24:27], v[48:51]
	v_mfma_f32_16x16x32_bf16 v[52:55], v[72:75], v[28:31], v[52:55]
	v_mfma_f32_16x16x32_bf16 v[48:51], v[80:83], v[32:35], v[48:51]
	v_mfma_f32_16x16x32_bf16 v[52:55], v[80:83], v[36:39], v[52:55]
	v_mfma_f32_16x16x32_bf16 v[48:51], v[88:91], v[40:43], v[48:51]
	v_mfma_f32_16x16x32_bf16 v[52:55], v[88:91], v[44:47], v[52:55]
	ds_read_b128 v[16:19], v63 offset:256
	ds_read_b128 v[20:23], v63 offset:8704
	ds_read_b128 v[24:27], v63 offset:320
	ds_read_b128 v[28:31], v63 offset:8768
	ds_read_b128 v[32:35], v63 offset:384
	ds_read_b128 v[36:39], v63 offset:8832
	ds_read_b128 v[40:43], v63 offset:448
	ds_read_b128 v[44:47], v63 offset:8896
	s_waitcnt lgkmcnt(0)
	v_mfma_f32_16x16x32_bf16 v[48:51], v[96:99], v[16:19], v[48:51]
	v_mfma_f32_16x16x32_bf16 v[52:55], v[96:99], v[20:23], v[52:55]
	v_mfma_f32_16x16x32_bf16 v[48:51], v[104:107], v[24:27], v[48:51]
	v_mfma_f32_16x16x32_bf16 v[52:55], v[104:107], v[28:31], v[52:55]
	v_mfma_f32_16x16x32_bf16 v[48:51], v[112:115], v[32:35], v[48:51]
	v_mfma_f32_16x16x32_bf16 v[52:55], v[112:115], v[36:39], v[52:55]
	v_mfma_f32_16x16x32_bf16 v[48:51], v[120:123], v[40:43], v[48:51]
	v_mfma_f32_16x16x32_bf16 v[52:55], v[120:123], v[44:47], v[52:55]
	s_nop 9
	s_lshr_b32 s58, s22, 3
	s_and_b32 s59, s22, 7
	s_lshr_b32 s60, s25, 4
	s_cmp_lg_u32 s24, 0
	s_cbranch_scc1 .Lpre_E_notq
	s_lshl_b32 s61, s22, 15
	s_lshl_b32 s37, s25, 2
	s_add_u32 s61, s61, s37
	s_add_u32 s62, s16, s61
	s_addc_u32 s63, s17, 0
	v_lshl_or_b32 v60, v2, 10, v14
	global_store_dwordx4 v60, v[48:51], s[62:63]
	s_add_u32 s62, s62, 0x4000
	s_addc_u32 s63, s63, 0
	global_store_dwordx4 v60, v[52:55], s[62:63]
	s_endpgm
